# mixer SGU step B: the 16 per-row bias loads of a lane issued in one batch (on top of the converter copy-out batching and the P6 table reuse)
# baseline (speedup 1.0000x reference)
; __device__ __forceinline__ float bf16_lo(unsigned u) { return __uint_as_float(u << 16); }
; __device__ __forceinline__ float bf16_hi(unsigned u) { return __uint_as_float(u & 0xffff0000u); }
; __device__ __forceinline__ void phase_mixer(const Params& p, LAS3 char* lds, int wid) {
;     ...
;                 const bf16_t* ub = proj + (size_t)t0 * DIN + 3072 + hd * 128 + 4 * n + cp;
;                 float ya[16], yb[16];
; #pragma unroll
;                 for (int r = 0; r < 16; ++r) {
;                     const int tt = 32 * mt + (r & 3) + 8 * (r >> 2) + 4 * kh;
;                     const unsigned uu = *(const unsigned*)(ub + (size_t)tt * DIN);
;                     const float bias = p.sgu_b[hd * 128 + tt];
;                     ya[r] = gelu_f(bf16_lo(uu)) * (acc0[r] + bias);
;                     yb[r] = gelu_f(bf16_hi(uu)) * (acc1[r] + bias);
;                     const float ps = half_sum32(ya[r] * ya[r] + yb[r] * yb[r]);
;                     if (n == 0) stat[tt * 2 + (wid & 1)] = ps;
.LBB0_179:
	s_mul_i32 s5, s94, 0x2800
	s_mul_hi_i32 s4, s94, 0x2800
	s_add_u32 s5, s56, s5
	s_addc_u32 s6, s57, s4
	s_lshl_b32 s10, s92, 1
	s_add_u32 s4, s5, s10
	s_addc_u32 s5, s6, 0
	v_lshl_add_u64 v[80:81], s[4:5], 0, v[36:37]
	s_lshl_b32 s26, s23, 1
	v_add_u32_e32 v82, s92, v94
	v_lshl_add_u64 v[80:81], v[80:81], 0, s[26:27]
	s_mov_b64 s[4:5], 0x1800
	v_ashrrev_i32_e32 v83, 31, v82
	v_lshl_add_u64 v[80:81], v[80:81], 0, s[4:5]
	v_lshl_add_u64 v[232:233], v[80:81], 0, v[40:41]
	global_load_dword v200, v[232:233], off
	v_lshl_add_u64 v[232:233], v[80:81], 0, v[42:43]
	global_load_dword v201, v[232:233], off
	v_lshl_add_u64 v[232:233], v[80:81], 0, v[44:45]
	global_load_dword v202, v[232:233], off
	v_lshl_add_u64 v[232:233], v[80:81], 0, v[46:47]
	global_load_dword v203, v[232:233], off
	v_lshl_add_u64 v[232:233], v[80:81], 0, v[48:49]
	global_load_dword v204, v[232:233], off
	v_lshl_add_u64 v[232:233], v[80:81], 0, v[50:51]
	global_load_dword v205, v[232:233], off
	v_lshl_add_u64 v[232:233], v[80:81], 0, v[52:53]
	global_load_dword v206, v[232:233], off
	v_lshl_add_u64 v[232:233], v[80:81], 0, v[54:55]
	global_load_dword v207, v[232:233], off
	v_lshl_add_u64 v[232:233], v[80:81], 0, v[56:57]
	global_load_dword v208, v[232:233], off
	v_lshl_add_u64 v[232:233], v[80:81], 0, v[62:63]
	global_load_dword v209, v[232:233], off
	v_lshl_add_u64 v[232:233], v[80:81], 0, v[64:65]
	global_load_dword v210, v[232:233], off
	v_lshl_add_u64 v[232:233], v[80:81], 0, v[66:67]
	global_load_dword v211, v[232:233], off
	v_lshl_add_u64 v[232:233], v[80:81], 0, v[68:69]
	global_load_dword v212, v[232:233], off
	v_lshl_add_u64 v[232:233], v[80:81], 0, v[70:71]
	global_load_dword v213, v[232:233], off
	v_lshl_add_u64 v[232:233], v[80:81], 0, v[72:73]
	global_load_dword v214, v[232:233], off
	v_lshl_add_u64 v[232:233], v[80:81], 0, v[74:75]
	global_load_dword v215, v[232:233], off
	v_lshl_add_u64 v[82:83], v[82:83], 2, s[98:99]
	global_load_dword v84, v[82:83], off
	global_load_dword v217, v[82:83], off offset:4
	global_load_dword v218, v[82:83], off offset:8
	global_load_dword v219, v[82:83], off offset:12
	global_load_dword v220, v[82:83], off offset:32
	global_load_dword v221, v[82:83], off offset:36
	global_load_dword v222, v[82:83], off offset:40
	global_load_dword v223, v[82:83], off offset:44
	global_load_dword v224, v[82:83], off offset:64
	global_load_dword v225, v[82:83], off offset:68
	global_load_dword v226, v[82:83], off offset:72
	global_load_dword v227, v[82:83], off offset:76
	global_load_dword v228, v[82:83], off offset:96
	global_load_dword v229, v[82:83], off offset:100
	global_load_dword v230, v[82:83], off offset:104
	global_load_dword v231, v[82:83], off offset:108
	v_lshl_add_u64 v[82:83], v[80:81], 0, v[40:41]
	s_waitcnt vmcnt(0)
	v_mov_b32_e32 v82, v200
	v_add_f32_e32 v16, v16, v84
	v_add_f32_e32 v0, v0, v84
	s_waitcnt vmcnt(0)
	v_lshlrev_b32_e32 v83, 16, v82
	v_and_b32_e32 v82, 0xffff0000, v82
	v_fma_f32 v84, |v83|, s87, 1.0
	v_fma_f32 v86, |v82|, s87, 1.0
	v_rcp_f32_e32 v84, v84
	v_rcp_f32_e32 v86, v86
	v_mul_f32_e32 v85, v83, v83
	v_mul_f32_e32 v87, v82, v82
	v_mul_f32_e32 v85, 0xbf38aa3b, v85
	v_fmamk_f32 v88, v84, 0x3f07dc22, v126
	v_mul_f32_e32 v87, 0xbf38aa3b, v87
	v_exp_f32_e32 v85, v85
	v_fmamk_f32 v89, v86, 0x3f07dc22, v126
	v_fmaak_f32 v88, v84, v88, 0x3f35f0e3
	v_exp_f32_e32 v87, v87
	v_fmaak_f32 v89, v86, v89, 0x3f35f0e3
	v_fmaak_f32 v88, v84, v88, 0xbe11a98e
	v_fmaak_f32 v89, v86, v89, 0xbe11a98e
	v_fmaak_f32 v88, v84, v88, 0x3e027906
	v_fmaak_f32 v89, v86, v89, 0x3e027906
	v_mul_f32_e32 v84, v84, v88
	v_mul_f32_e32 v86, v86, v89
	v_mul_f32_e32 v84, v85, v84
	v_mul_f32_e32 v85, v87, v86
	v_mul_f32_e32 v86, v84, v83
	v_fma_f32 v84, -v84, v83, v83
	v_cmp_gt_f32_e32 vcc, 0, v83
	v_mul_f32_e32 v87, v85, v82
	v_fma_f32 v85, -v85, v82, v82
	v_cndmask_b32_e32 v83, v84, v86, vcc
	v_cmp_gt_f32_e32 vcc, 0, v82
	v_mul_f32_e32 v16, v16, v83
	s_nop 0
	v_cndmask_b32_e32 v82, v85, v87, vcc
	v_mul_f32_e32 v84, v0, v82
	v_mul_f32_e32 v0, v84, v84
	v_fmac_f32_e32 v0, v16, v16
	s_nop 1
	s_waitcnt lgkmcnt(0)
	v_add_f32_dpp v0, v0, v0 quad_perm:[1,0,3,2] row_mask:0xf bank_mask:0xf
	s_nop 1
	s_waitcnt lgkmcnt(0)
	v_add_f32_dpp v0, v0, v0 quad_perm:[2,3,0,1] row_mask:0xf bank_mask:0xf
	s_nop 1
	s_waitcnt lgkmcnt(0)
	v_add_f32_dpp v0, v0, v0 row_half_mirror row_mask:0xf bank_mask:0xf
	s_nop 1
	s_waitcnt lgkmcnt(0)
	v_add_f32_dpp v0, v0, v0 row_mirror row_mask:0xf bank_mask:0xf
	ds_swizzle_b32 v82, v0 offset:swizzle(SWAP,16)
	s_and_saveexec_b64 s[4:5], s[0:1]
	s_cbranch_execz .LBB0_181
	s_waitcnt lgkmcnt(0)
	v_add_f32_e32 v0, v0, v82
	v_add_u32_e32 v82, s25, v95
	ds_write_b32 v82, v0 offset:32768
; __device__ __forceinline__ float bf16_lo(unsigned u) { return __uint_as_float(u << 16); }
; __device__ __forceinline__ float bf16_hi(unsigned u) { return __uint_as_float(u & 0xffff0000u); }
; __device__ __forceinline__ void phase_mixer(const Params& p, LAS3 char* lds, int wid) {
;     ...
;                 for (int r = 0; r < 16; ++r) {
;                     const int tt = 32 * mt + (r & 3) + 8 * (r >> 2) + 4 * kh;
;                     const unsigned uu = *(const unsigned*)(ub + (size_t)tt * DIN);
;                     const float bias = p.sgu_b[hd * 128 + tt];
;                     ya[r] = gelu_f(bf16_lo(uu)) * (acc0[r] + bias);
;                     yb[r] = gelu_f(bf16_hi(uu)) * (acc1[r] + bias);
;                     const float ps = half_sum32(ya[r] * ya[r] + yb[r] * yb[r]);
;                     if (n == 0) stat[tt * 2 + (wid & 1)] = ps;
.LBB0_181:
	s_or_b64 exec, exec, s[4:5]
	s_waitcnt lgkmcnt(0)
	v_lshl_add_u64 v[82:83], v[80:81], 0, v[42:43]
	v_lshl_add_u64 v[82:83], s[92:93], 0, v[60:61]
	v_lshl_add_u64 v[82:83], v[82:83], 2, s[98:99]
	v_mov_b32_e32 v85, v217
	s_waitcnt vmcnt(0)
	v_mov_b32_e32 v0, v201
	v_lshlrev_b32_e32 v86, 16, v0
	v_and_b32_e32 v0, 0xffff0000, v0
	v_fma_f32 v87, |v86|, s87, 1.0
	v_mul_f32_e32 v88, v86, v86
	s_waitcnt vmcnt(0)
	v_add_f32_e32 v17, v17, v85
	v_fma_f32 v89, |v0|, s87, 1.0
	v_add_f32_e32 v1, v1, v85
	v_rcp_f32_e32 v85, v87
	v_mul_f32_e32 v87, 0xbf38aa3b, v88
	v_rcp_f32_e32 v88, v89
	v_mul_f32_e32 v90, v0, v0
	v_mul_f32_e32 v89, 0xbf38aa3b, v90
	v_fmamk_f32 v90, v85, 0x3f07dc22, v126
	v_exp_f32_e32 v87, v87
	v_fmamk_f32 v91, v88, 0x3f07dc22, v126
	v_fmaak_f32 v90, v85, v90, 0x3f35f0e3
	v_exp_f32_e32 v89, v89
	v_fmaak_f32 v91, v88, v91, 0x3f35f0e3
	v_fmaak_f32 v90, v85, v90, 0xbe11a98e
	v_fmaak_f32 v91, v88, v91, 0xbe11a98e
	v_fmaak_f32 v90, v85, v90, 0x3e027906
	v_fmaak_f32 v91, v88, v91, 0x3e027906
	v_mul_f32_e32 v85, v85, v90
	v_mul_f32_e32 v88, v88, v91
	v_mul_f32_e32 v85, v87, v85
	v_mul_f32_e32 v87, v89, v88
	v_mul_f32_e32 v88, v85, v86
	v_fma_f32 v85, -v85, v86, v86
	v_cmp_gt_f32_e32 vcc, 0, v86
	v_mul_f32_e32 v89, v87, v0
	v_fma_f32 v87, -v87, v0, v0
	v_cndmask_b32_e32 v85, v85, v88, vcc
	v_cmp_gt_f32_e32 vcc, 0, v0
	v_mul_f32_e32 v17, v17, v85
	s_nop 0
	v_cndmask_b32_e32 v0, v87, v89, vcc
	v_mul_f32_e32 v85, v1, v0
	v_mul_f32_e32 v0, v85, v85
	v_fmac_f32_e32 v0, v17, v17
	s_nop 1
	s_waitcnt lgkmcnt(0)
	v_add_f32_dpp v0, v0, v0 quad_perm:[1,0,3,2] row_mask:0xf bank_mask:0xf
	s_nop 1
	s_waitcnt lgkmcnt(0)
	v_add_f32_dpp v0, v0, v0 quad_perm:[2,3,0,1] row_mask:0xf bank_mask:0xf
	s_nop 1
	s_waitcnt lgkmcnt(0)
	v_add_f32_dpp v0, v0, v0 row_half_mirror row_mask:0xf bank_mask:0xf
	s_nop 1
	s_waitcnt lgkmcnt(0)
	v_add_f32_dpp v0, v0, v0 row_mirror row_mask:0xf bank_mask:0xf
	ds_swizzle_b32 v1, v0 offset:swizzle(SWAP,16)
	s_and_saveexec_b64 s[4:5], s[0:1]
	s_cbranch_execz .LBB0_183
	s_waitcnt lgkmcnt(0)
	v_add_f32_e32 v0, v0, v1
	v_add_u32_e32 v1, s25, v97
	ds_write_b32 v1, v0 offset:32768
.LBB0_183:
	s_or_b64 exec, exec, s[4:5]
	s_waitcnt lgkmcnt(0)
	v_lshl_add_u64 v[0:1], v[80:81], 0, v[44:45]
	v_mov_b32_e32 v86, v218
	s_nop 0
	s_waitcnt vmcnt(0)
	v_mov_b32_e32 v0, v202
	v_add_f32_e32 v1, v18, v86
	v_add_f32_e32 v18, v2, v86
	s_waitcnt vmcnt(0)
	v_lshlrev_b32_e32 v2, 16, v0
	v_and_b32_e32 v0, 0xffff0000, v0
	v_fma_f32 v86, |v2|, s87, 1.0
	v_fma_f32 v88, |v0|, s87, 1.0
	v_rcp_f32_e32 v86, v86
	v_rcp_f32_e32 v88, v88
	v_mul_f32_e32 v87, v2, v2
	v_mul_f32_e32 v89, v0, v0
	v_mul_f32_e32 v87, 0xbf38aa3b, v87
	v_fmamk_f32 v90, v86, 0x3f07dc22, v126
	v_mul_f32_e32 v89, 0xbf38aa3b, v89
	v_exp_f32_e32 v87, v87
	v_fmamk_f32 v91, v88, 0x3f07dc22, v126
	v_fmaak_f32 v90, v86, v90, 0x3f35f0e3
	v_exp_f32_e32 v89, v89
	v_fmaak_f32 v91, v88, v91, 0x3f35f0e3
	v_fmaak_f32 v90, v86, v90, 0xbe11a98e
	v_fmaak_f32 v91, v88, v91, 0xbe11a98e
	v_fmaak_f32 v90, v86, v90, 0x3e027906
	v_fmaak_f32 v91, v88, v91, 0x3e027906
	v_mul_f32_e32 v86, v86, v90
	v_mul_f32_e32 v88, v88, v91
	v_mul_f32_e32 v86, v87, v86
	v_mul_f32_e32 v87, v89, v88
	v_mul_f32_e32 v88, v86, v2
	v_fma_f32 v86, -v86, v2, v2
	v_cmp_gt_f32_e32 vcc, 0, v2
	v_mul_f32_e32 v89, v87, v0
	v_fma_f32 v87, -v87, v0, v0
	v_cndmask_b32_e32 v2, v86, v88, vcc
	v_cmp_gt_f32_e32 vcc, 0, v0
	v_mul_f32_e32 v2, v1, v2
	s_nop 0
	v_cndmask_b32_e32 v0, v87, v89, vcc
	v_mul_f32_e32 v18, v18, v0
	v_mul_f32_e32 v0, v18, v18
	v_fmac_f32_e32 v0, v2, v2
	s_nop 1
	s_waitcnt lgkmcnt(0)
	v_add_f32_dpp v0, v0, v0 quad_perm:[1,0,3,2] row_mask:0xf bank_mask:0xf
	s_nop 1
	s_waitcnt lgkmcnt(0)
	v_add_f32_dpp v0, v0, v0 quad_perm:[2,3,0,1] row_mask:0xf bank_mask:0xf
	s_nop 1
	s_waitcnt lgkmcnt(0)
	v_add_f32_dpp v0, v0, v0 row_half_mirror row_mask:0xf bank_mask:0xf
	s_nop 1
	s_waitcnt lgkmcnt(0)
	v_add_f32_dpp v0, v0, v0 row_mirror row_mask:0xf bank_mask:0xf
	ds_swizzle_b32 v1, v0 offset:swizzle(SWAP,16)
	s_and_saveexec_b64 s[4:5], s[0:1]
	s_cbranch_execz .LBB0_185
	s_waitcnt lgkmcnt(0)
	v_add_f32_e32 v0, v0, v1
	v_add_u32_e32 v1, s25, v99
	ds_write_b32 v1, v0 offset:32768
.LBB0_185:
	s_or_b64 exec, exec, s[4:5]
	s_waitcnt lgkmcnt(0)
	v_lshl_add_u64 v[0:1], v[80:81], 0, v[46:47]
	v_mov_b32_e32 v86, v219
	s_waitcnt vmcnt(0)
	v_add_f32_e32 v3, v3, v86
	v_add_f32_e32 v1, v19, v86
	s_waitcnt vmcnt(0)
	v_mov_b32_e32 v0, v203
	v_lshlrev_b32_e32 v19, 16, v0
	v_and_b32_e32 v0, 0xffff0000, v0
	v_fma_f32 v86, |v19|, s87, 1.0
	v_fma_f32 v88, |v0|, s87, 1.0
	v_rcp_f32_e32 v86, v86
	v_rcp_f32_e32 v88, v88
	v_mul_f32_e32 v87, v19, v19
	v_mul_f32_e32 v89, v0, v0
	v_mul_f32_e32 v87, 0xbf38aa3b, v87
	v_fmamk_f32 v90, v86, 0x3f07dc22, v126
	v_mul_f32_e32 v89, 0xbf38aa3b, v89
	v_exp_f32_e32 v87, v87
	v_fmamk_f32 v91, v88, 0x3f07dc22, v126
	v_fmaak_f32 v90, v86, v90, 0x3f35f0e3
	v_exp_f32_e32 v89, v89
	v_fmaak_f32 v91, v88, v91, 0x3f35f0e3
	v_fmaak_f32 v90, v86, v90, 0xbe11a98e
	v_fmaak_f32 v91, v88, v91, 0xbe11a98e
	v_fmaak_f32 v90, v86, v90, 0x3e027906
	v_fmaak_f32 v91, v88, v91, 0x3e027906
	v_mul_f32_e32 v86, v86, v90
	v_mul_f32_e32 v88, v88, v91
	v_mul_f32_e32 v86, v87, v86
	v_mul_f32_e32 v87, v89, v88
	v_mul_f32_e32 v88, v86, v19
	v_fma_f32 v86, -v86, v19, v19
	v_cmp_gt_f32_e32 vcc, 0, v19
	v_mul_f32_e32 v89, v87, v0
	v_fma_f32 v87, -v87, v0, v0
	v_cndmask_b32_e32 v19, v86, v88, vcc
	v_cmp_gt_f32_e32 vcc, 0, v0
	v_mul_f32_e32 v19, v1, v19
	s_nop 0
	v_cndmask_b32_e32 v0, v87, v89, vcc
	v_mul_f32_e32 v3, v3, v0
	v_mul_f32_e32 v0, v3, v3
	v_fmac_f32_e32 v0, v19, v19
	s_nop 1
	s_waitcnt lgkmcnt(0)
	v_add_f32_dpp v0, v0, v0 quad_perm:[1,0,3,2] row_mask:0xf bank_mask:0xf
	s_nop 1
	s_waitcnt lgkmcnt(0)
	v_add_f32_dpp v0, v0, v0 quad_perm:[2,3,0,1] row_mask:0xf bank_mask:0xf
	s_nop 1
	s_waitcnt lgkmcnt(0)
	v_add_f32_dpp v0, v0, v0 row_half_mirror row_mask:0xf bank_mask:0xf
	s_nop 1
	s_waitcnt lgkmcnt(0)
	v_add_f32_dpp v0, v0, v0 row_mirror row_mask:0xf bank_mask:0xf
	ds_swizzle_b32 v1, v0 offset:swizzle(SWAP,16)
	s_and_saveexec_b64 s[4:5], s[0:1]
	s_cbranch_execz .LBB0_187
	s_waitcnt lgkmcnt(0)
	v_add_f32_e32 v0, v0, v1
	v_add_u32_e32 v1, s25, v101
	ds_write_b32 v1, v0 offset:32768
; __device__ __forceinline__ float bf16_lo(unsigned u) { return __uint_as_float(u << 16); }
; __device__ __forceinline__ float bf16_hi(unsigned u) { return __uint_as_float(u & 0xffff0000u); }
; __device__ __forceinline__ float gelu_f(float v) {
;     const float av = fabsf(v), dd = av * 0.2316418882f + 1.0f;
;     const float tt = __builtin_amdgcn_rcpf(dd);
;     float q = tt * 0.5307027145f + (-0.7265760135f); q = q * tt + 0.7107068705f; q = q * tt + (-0.142248368f); q = q * tt + 0.127414796f; q = q * tt;
;     const float e = __builtin_amdgcn_exp2f((v * v) * (-0.72134752044f));
;     const float m = v * (q * e);
;     return v < 0.f ? m : v - m;
; __device__ __forceinline__ void phase_mixer(const Params& p, LAS3 char* lds, int wid) {
;     ...
;                 for (int r = 0; r < 16; ++r) {
;                     const int tt = 32 * mt + (r & 3) + 8 * (r >> 2) + 4 * kh;
;                     const unsigned uu = *(const unsigned*)(ub + (size_t)tt * DIN);
;                     const float bias = p.sgu_b[hd * 128 + tt];
;                     ya[r] = gelu_f(bf16_lo(uu)) * (acc0[r] + bias);
;                     yb[r] = gelu_f(bf16_hi(uu)) * (acc1[r] + bias);
;                     const float ps = half_sum32(ya[r] * ya[r] + yb[r] * yb[r]);
;                     if (n == 0) stat[tt * 2 + (wid & 1)] = ps;
;                 }
.LBB0_187:
	s_or_b64 exec, exec, s[4:5]
	s_waitcnt lgkmcnt(0)
	v_lshl_add_u64 v[0:1], v[80:81], 0, v[48:49]
	v_mov_b32_e32 v86, v220
	s_waitcnt vmcnt(0)
	v_add_f32_e32 v4, v4, v86
	v_add_f32_e32 v1, v20, v86
	s_waitcnt vmcnt(0)
	v_mov_b32_e32 v0, v204
	v_lshlrev_b32_e32 v20, 16, v0
	v_and_b32_e32 v0, 0xffff0000, v0
	v_fma_f32 v86, |v20|, s87, 1.0
	v_fma_f32 v88, |v0|, s87, 1.0
	v_rcp_f32_e32 v86, v86
	v_rcp_f32_e32 v88, v88
	v_mul_f32_e32 v87, v20, v20
	v_mul_f32_e32 v89, v0, v0
	v_mul_f32_e32 v87, 0xbf38aa3b, v87
	v_fmamk_f32 v90, v86, 0x3f07dc22, v126
	v_mul_f32_e32 v89, 0xbf38aa3b, v89
	v_exp_f32_e32 v87, v87
	v_fmamk_f32 v91, v88, 0x3f07dc22, v126
	v_fmaak_f32 v90, v86, v90, 0x3f35f0e3
	v_exp_f32_e32 v89, v89
	v_fmaak_f32 v91, v88, v91, 0x3f35f0e3
	v_fmaak_f32 v90, v86, v90, 0xbe11a98e
	v_fmaak_f32 v91, v88, v91, 0xbe11a98e
	v_fmaak_f32 v90, v86, v90, 0x3e027906
	v_fmaak_f32 v91, v88, v91, 0x3e027906
	v_mul_f32_e32 v86, v86, v90
	v_mul_f32_e32 v88, v88, v91
	v_mul_f32_e32 v86, v87, v86
	v_mul_f32_e32 v87, v89, v88
	v_mul_f32_e32 v88, v86, v20
	v_fma_f32 v86, -v86, v20, v20
	v_cmp_gt_f32_e32 vcc, 0, v20
	v_mul_f32_e32 v89, v87, v0
	v_fma_f32 v87, -v87, v0, v0
	v_cndmask_b32_e32 v20, v86, v88, vcc
	v_cmp_gt_f32_e32 vcc, 0, v0
	v_mul_f32_e32 v20, v1, v20
	s_nop 0
	v_cndmask_b32_e32 v0, v87, v89, vcc
	v_mul_f32_e32 v4, v4, v0
	v_mul_f32_e32 v0, v4, v4
	v_fmac_f32_e32 v0, v20, v20
	s_nop 1
	s_waitcnt lgkmcnt(0)
	v_add_f32_dpp v0, v0, v0 quad_perm:[1,0,3,2] row_mask:0xf bank_mask:0xf
	s_nop 1
	s_waitcnt lgkmcnt(0)
	v_add_f32_dpp v0, v0, v0 quad_perm:[2,3,0,1] row_mask:0xf bank_mask:0xf
	s_nop 1
	s_waitcnt lgkmcnt(0)
	v_add_f32_dpp v0, v0, v0 row_half_mirror row_mask:0xf bank_mask:0xf
	s_nop 1
	s_waitcnt lgkmcnt(0)
	v_add_f32_dpp v0, v0, v0 row_mirror row_mask:0xf bank_mask:0xf
	ds_swizzle_b32 v1, v0 offset:swizzle(SWAP,16)
	s_and_saveexec_b64 s[4:5], s[0:1]
	s_cbranch_execz .LBB0_189
	s_waitcnt lgkmcnt(0)
	v_add_f32_e32 v0, v0, v1
	v_add_u32_e32 v1, s25, v103
	ds_write_b32 v1, v0 offset:32768
.LBB0_189:
	s_or_b64 exec, exec, s[4:5]
	s_waitcnt lgkmcnt(0)
	v_lshl_add_u64 v[0:1], v[80:81], 0, v[50:51]
	v_mov_b32_e32 v86, v221
	s_waitcnt vmcnt(0)
	v_add_f32_e32 v5, v5, v86
	v_add_f32_e32 v1, v21, v86
	s_waitcnt vmcnt(0)
	v_mov_b32_e32 v0, v205
	v_lshlrev_b32_e32 v21, 16, v0
	v_and_b32_e32 v0, 0xffff0000, v0
	v_fma_f32 v86, |v21|, s87, 1.0
	v_fma_f32 v88, |v0|, s87, 1.0
	v_rcp_f32_e32 v86, v86
	v_rcp_f32_e32 v88, v88
	v_mul_f32_e32 v87, v21, v21
	v_mul_f32_e32 v89, v0, v0
	v_mul_f32_e32 v87, 0xbf38aa3b, v87
	v_fmamk_f32 v90, v86, 0x3f07dc22, v126
	v_mul_f32_e32 v89, 0xbf38aa3b, v89
	v_exp_f32_e32 v87, v87
	v_fmamk_f32 v91, v88, 0x3f07dc22, v126
	v_fmaak_f32 v90, v86, v90, 0x3f35f0e3
	v_exp_f32_e32 v89, v89
	v_fmaak_f32 v91, v88, v91, 0x3f35f0e3
	v_fmaak_f32 v90, v86, v90, 0xbe11a98e
	v_fmaak_f32 v91, v88, v91, 0xbe11a98e
	v_fmaak_f32 v90, v86, v90, 0x3e027906
	v_fmaak_f32 v91, v88, v91, 0x3e027906
	v_mul_f32_e32 v86, v86, v90
	v_mul_f32_e32 v88, v88, v91
	v_mul_f32_e32 v86, v87, v86
	v_mul_f32_e32 v87, v89, v88
	v_mul_f32_e32 v88, v86, v21
	v_fma_f32 v86, -v86, v21, v21
	v_cmp_gt_f32_e32 vcc, 0, v21
	v_mul_f32_e32 v89, v87, v0
	v_fma_f32 v87, -v87, v0, v0
	v_cndmask_b32_e32 v21, v86, v88, vcc
	v_cmp_gt_f32_e32 vcc, 0, v0
	v_mul_f32_e32 v21, v1, v21
	s_nop 0
	v_cndmask_b32_e32 v0, v87, v89, vcc
	v_mul_f32_e32 v5, v5, v0
	v_mul_f32_e32 v0, v5, v5
	v_fmac_f32_e32 v0, v21, v21
	s_nop 1
	s_waitcnt lgkmcnt(0)
	v_add_f32_dpp v0, v0, v0 quad_perm:[1,0,3,2] row_mask:0xf bank_mask:0xf
	s_nop 1
	s_waitcnt lgkmcnt(0)
	v_add_f32_dpp v0, v0, v0 quad_perm:[2,3,0,1] row_mask:0xf bank_mask:0xf
	s_nop 1
	s_waitcnt lgkmcnt(0)
	v_add_f32_dpp v0, v0, v0 row_half_mirror row_mask:0xf bank_mask:0xf
	s_nop 1
	s_waitcnt lgkmcnt(0)
	v_add_f32_dpp v0, v0, v0 row_mirror row_mask:0xf bank_mask:0xf
	ds_swizzle_b32 v1, v0 offset:swizzle(SWAP,16)
	s_and_saveexec_b64 s[4:5], s[0:1]
	s_cbranch_execz .LBB0_191
	s_waitcnt lgkmcnt(0)
	v_add_f32_e32 v0, v0, v1
	v_add_u32_e32 v1, s25, v105
	ds_write_b32 v1, v0 offset:32768
.LBB0_191:
	s_or_b64 exec, exec, s[4:5]
	s_waitcnt lgkmcnt(0)
	v_lshl_add_u64 v[0:1], v[80:81], 0, v[52:53]
	v_mov_b32_e32 v86, v222
	s_waitcnt vmcnt(0)
	v_add_f32_e32 v6, v6, v86
	v_add_f32_e32 v1, v22, v86
	s_waitcnt vmcnt(0)
	v_mov_b32_e32 v0, v206
	v_lshlrev_b32_e32 v22, 16, v0
	v_and_b32_e32 v0, 0xffff0000, v0
	v_fma_f32 v86, |v22|, s87, 1.0
	v_fma_f32 v88, |v0|, s87, 1.0
	v_rcp_f32_e32 v86, v86
	v_rcp_f32_e32 v88, v88
	v_mul_f32_e32 v87, v22, v22
	v_mul_f32_e32 v89, v0, v0
	v_mul_f32_e32 v87, 0xbf38aa3b, v87
	v_fmamk_f32 v90, v86, 0x3f07dc22, v126
	v_mul_f32_e32 v89, 0xbf38aa3b, v89
	v_exp_f32_e32 v87, v87
	v_fmamk_f32 v91, v88, 0x3f07dc22, v126
	v_fmaak_f32 v90, v86, v90, 0x3f35f0e3
	v_exp_f32_e32 v89, v89
	v_fmaak_f32 v91, v88, v91, 0x3f35f0e3
	v_fmaak_f32 v90, v86, v90, 0xbe11a98e
	v_fmaak_f32 v91, v88, v91, 0xbe11a98e
	v_fmaak_f32 v90, v86, v90, 0x3e027906
	v_fmaak_f32 v91, v88, v91, 0x3e027906
	v_mul_f32_e32 v86, v86, v90
	v_mul_f32_e32 v88, v88, v91
	v_mul_f32_e32 v86, v87, v86
	v_mul_f32_e32 v87, v89, v88
	v_mul_f32_e32 v88, v86, v22
	v_fma_f32 v86, -v86, v22, v22
	v_cmp_gt_f32_e32 vcc, 0, v22
	v_mul_f32_e32 v89, v87, v0
	v_fma_f32 v87, -v87, v0, v0
	v_cndmask_b32_e32 v22, v86, v88, vcc
	v_cmp_gt_f32_e32 vcc, 0, v0
	v_mul_f32_e32 v22, v1, v22
	s_nop 0
	v_cndmask_b32_e32 v0, v87, v89, vcc
	v_mul_f32_e32 v6, v6, v0
	v_mul_f32_e32 v0, v6, v6
	v_fmac_f32_e32 v0, v22, v22
	s_nop 1
	s_waitcnt lgkmcnt(0)
	v_add_f32_dpp v0, v0, v0 quad_perm:[1,0,3,2] row_mask:0xf bank_mask:0xf
	s_nop 1
	s_waitcnt lgkmcnt(0)
	v_add_f32_dpp v0, v0, v0 quad_perm:[2,3,0,1] row_mask:0xf bank_mask:0xf
	s_nop 1
	s_waitcnt lgkmcnt(0)
	v_add_f32_dpp v0, v0, v0 row_half_mirror row_mask:0xf bank_mask:0xf
	s_nop 1
	s_waitcnt lgkmcnt(0)
	v_add_f32_dpp v0, v0, v0 row_mirror row_mask:0xf bank_mask:0xf
	ds_swizzle_b32 v1, v0 offset:swizzle(SWAP,16)
	s_and_saveexec_b64 s[4:5], s[0:1]
	s_cbranch_execz .LBB0_193
	s_waitcnt lgkmcnt(0)
	v_add_f32_e32 v0, v0, v1
	v_add_u32_e32 v1, s25, v107
	ds_write_b32 v1, v0 offset:32768
; __device__ __forceinline__ float bf16_lo(unsigned u) { return __uint_as_float(u << 16); }
; __device__ __forceinline__ float bf16_hi(unsigned u) { return __uint_as_float(u & 0xffff0000u); }
; __device__ __forceinline__ float gelu_f(float v) {
;     const float av = fabsf(v), dd = av * 0.2316418882f + 1.0f;
;     const float tt = __builtin_amdgcn_rcpf(dd);
;     float q = tt * 0.5307027145f + (-0.7265760135f); q = q * tt + 0.7107068705f; q = q * tt + (-0.142248368f); q = q * tt + 0.127414796f; q = q * tt;
;     const float e = __builtin_amdgcn_exp2f((v * v) * (-0.72134752044f));
;     const float m = v * (q * e);
;     return v < 0.f ? m : v - m;
; __device__ __forceinline__ void phase_mixer(const Params& p, LAS3 char* lds, int wid) {
;     ...
;                 for (int r = 0; r < 16; ++r) {
;                     const int tt = 32 * mt + (r & 3) + 8 * (r >> 2) + 4 * kh;
;                     const unsigned uu = *(const unsigned*)(ub + (size_t)tt * DIN);
;                     const float bias = p.sgu_b[hd * 128 + tt];
;                     ya[r] = gelu_f(bf16_lo(uu)) * (acc0[r] + bias);
;                     yb[r] = gelu_f(bf16_hi(uu)) * (acc1[r] + bias);
;                     const float ps = half_sum32(ya[r] * ya[r] + yb[r] * yb[r]);
;                     if (n == 0) stat[tt * 2 + (wid & 1)] = ps;
;                 }
.LBB0_193:
	s_or_b64 exec, exec, s[4:5]
	s_waitcnt lgkmcnt(0)
	v_lshl_add_u64 v[0:1], v[80:81], 0, v[54:55]
	v_mov_b32_e32 v82, v223
	s_waitcnt vmcnt(0)
	v_add_f32_e32 v7, v7, v82
	v_add_f32_e32 v1, v23, v82
	s_waitcnt vmcnt(0)
	v_mov_b32_e32 v0, v207
	v_lshlrev_b32_e32 v23, 16, v0
	v_and_b32_e32 v0, 0xffff0000, v0
	v_fma_f32 v82, |v23|, s87, 1.0
	v_fma_f32 v86, |v0|, s87, 1.0
	v_rcp_f32_e32 v82, v82
	v_rcp_f32_e32 v86, v86
	v_mul_f32_e32 v83, v23, v23
	v_mul_f32_e32 v87, v0, v0
	v_mul_f32_e32 v83, 0xbf38aa3b, v83
	v_fmamk_f32 v88, v82, 0x3f07dc22, v126
	v_mul_f32_e32 v87, 0xbf38aa3b, v87
	v_exp_f32_e32 v83, v83
	v_fmamk_f32 v89, v86, 0x3f07dc22, v126
	v_fmaak_f32 v88, v82, v88, 0x3f35f0e3
	v_exp_f32_e32 v87, v87
	v_fmaak_f32 v89, v86, v89, 0x3f35f0e3
	v_fmaak_f32 v88, v82, v88, 0xbe11a98e
	v_fmaak_f32 v89, v86, v89, 0xbe11a98e
	v_fmaak_f32 v88, v82, v88, 0x3e027906
	v_fmaak_f32 v89, v86, v89, 0x3e027906
	v_mul_f32_e32 v82, v82, v88
	v_mul_f32_e32 v86, v86, v89
	v_mul_f32_e32 v82, v83, v82
	v_mul_f32_e32 v83, v87, v86
	v_mul_f32_e32 v86, v82, v23
	v_fma_f32 v82, -v82, v23, v23
	v_cmp_gt_f32_e32 vcc, 0, v23
	v_mul_f32_e32 v87, v83, v0
	v_fma_f32 v83, -v83, v0, v0
	v_cndmask_b32_e32 v23, v82, v86, vcc
	v_cmp_gt_f32_e32 vcc, 0, v0
	v_mul_f32_e32 v23, v1, v23
	s_nop 0
	v_cndmask_b32_e32 v0, v83, v87, vcc
	v_mul_f32_e32 v7, v7, v0
	v_mul_f32_e32 v0, v7, v7
	v_fmac_f32_e32 v0, v23, v23
	s_nop 1
	s_waitcnt lgkmcnt(0)
	v_add_f32_dpp v0, v0, v0 quad_perm:[1,0,3,2] row_mask:0xf bank_mask:0xf
	s_nop 1
	s_waitcnt lgkmcnt(0)
	v_add_f32_dpp v0, v0, v0 quad_perm:[2,3,0,1] row_mask:0xf bank_mask:0xf
	s_nop 1
	s_waitcnt lgkmcnt(0)
	v_add_f32_dpp v0, v0, v0 row_half_mirror row_mask:0xf bank_mask:0xf
	s_nop 1
	s_waitcnt lgkmcnt(0)
	v_add_f32_dpp v0, v0, v0 row_mirror row_mask:0xf bank_mask:0xf
	ds_swizzle_b32 v1, v0 offset:swizzle(SWAP,16)
	s_and_saveexec_b64 s[4:5], s[0:1]
	s_cbranch_execz .LBB0_195
	s_waitcnt lgkmcnt(0)
	v_add_f32_e32 v0, v0, v1
	v_add_u32_e32 v1, s25, v109
	ds_write_b32 v1, v0 offset:32768
.LBB0_195:
	s_or_b64 exec, exec, s[4:5]
	s_waitcnt lgkmcnt(0)
	v_lshl_add_u64 v[0:1], v[80:81], 0, v[56:57]
	v_add_u32_e32 v0, s92, v110
	v_ashrrev_i32_e32 v1, 31, v0
	v_lshl_add_u64 v[0:1], v[0:1], 2, s[98:99]
	v_mov_b32_e32 v0, v224
	s_waitcnt vmcnt(0)
	v_mov_b32_e32 v82, v208
	v_lshlrev_b32_e32 v1, 16, v82
	v_and_b32_e32 v82, 0xffff0000, v82
	v_fma_f32 v83, |v1|, s87, 1.0
	v_fma_f32 v87, |v82|, s87, 1.0
	v_rcp_f32_e32 v83, v83
	v_rcp_f32_e32 v87, v87
	v_mul_f32_e32 v86, v1, v1
	v_mul_f32_e32 v88, v82, v82
	v_mul_f32_e32 v86, 0xbf38aa3b, v86
	v_mul_f32_e32 v88, 0xbf38aa3b, v88
	s_waitcnt vmcnt(0)
	v_add_f32_e32 v24, v24, v0
	v_add_f32_e32 v0, v8, v0
	v_exp_f32_e32 v8, v86
	v_exp_f32_e32 v86, v88
	v_fmamk_f32 v88, v83, 0x3f07dc22, v126
	v_fmamk_f32 v89, v87, 0x3f07dc22, v126
	v_fmaak_f32 v88, v83, v88, 0x3f35f0e3
	v_fmaak_f32 v89, v87, v89, 0x3f35f0e3
	v_fmaak_f32 v88, v83, v88, 0xbe11a98e
	v_fmaak_f32 v89, v87, v89, 0xbe11a98e
	v_fmaak_f32 v88, v83, v88, 0x3e027906
	v_fmaak_f32 v89, v87, v89, 0x3e027906
	v_mul_f32_e32 v83, v83, v88
	v_mul_f32_e32 v87, v87, v89
	v_mul_f32_e32 v8, v8, v83
	v_mul_f32_e32 v83, v86, v87
	v_mul_f32_e32 v86, v8, v1
	v_fma_f32 v8, -v8, v1, v1
	v_cmp_gt_f32_e32 vcc, 0, v1
	v_mul_f32_e32 v87, v83, v82
	v_fma_f32 v83, -v83, v82, v82
	v_cndmask_b32_e32 v1, v8, v86, vcc
	v_cmp_gt_f32_e32 vcc, 0, v82
	v_mul_f32_e32 v24, v24, v1
	s_nop 0
	v_cndmask_b32_e32 v8, v83, v87, vcc
	v_mul_f32_e32 v8, v0, v8
	v_mul_f32_e32 v0, v8, v8
	v_fmac_f32_e32 v0, v24, v24
	s_nop 1
	s_waitcnt lgkmcnt(0)
	v_add_f32_dpp v0, v0, v0 quad_perm:[1,0,3,2] row_mask:0xf bank_mask:0xf
	s_nop 1
	s_waitcnt lgkmcnt(0)
	v_add_f32_dpp v0, v0, v0 quad_perm:[2,3,0,1] row_mask:0xf bank_mask:0xf
	s_nop 1
	s_waitcnt lgkmcnt(0)
	v_add_f32_dpp v0, v0, v0 row_half_mirror row_mask:0xf bank_mask:0xf
	s_nop 1
	s_waitcnt lgkmcnt(0)
	v_add_f32_dpp v0, v0, v0 row_mirror row_mask:0xf bank_mask:0xf
	ds_swizzle_b32 v1, v0 offset:swizzle(SWAP,16)
	s_and_saveexec_b64 s[4:5], s[0:1]
	s_cbranch_execz .LBB0_197
	s_waitcnt lgkmcnt(0)
	v_add_f32_e32 v0, v0, v1
	v_add_u32_e32 v1, s25, v111
	ds_write_b32 v1, v0 offset:32768
.LBB0_197:
	s_or_b64 exec, exec, s[4:5]
	s_waitcnt lgkmcnt(0)
	v_lshl_add_u64 v[0:1], v[80:81], 0, v[62:63]
	v_add_u32_e32 v0, s92, v112
	v_ashrrev_i32_e32 v1, 31, v0
	v_lshl_add_u64 v[0:1], v[0:1], 2, s[98:99]
	v_mov_b32_e32 v0, v225
	s_waitcnt vmcnt(0)
	v_mov_b32_e32 v82, v209
	v_lshlrev_b32_e32 v1, 16, v82
	v_and_b32_e32 v82, 0xffff0000, v82
	v_fma_f32 v83, |v1|, s87, 1.0
	v_fma_f32 v87, |v82|, s87, 1.0
	v_rcp_f32_e32 v83, v83
	v_rcp_f32_e32 v87, v87
	v_mul_f32_e32 v86, v1, v1
	v_mul_f32_e32 v88, v82, v82
	v_mul_f32_e32 v86, 0xbf38aa3b, v86
	v_mul_f32_e32 v88, 0xbf38aa3b, v88
	s_waitcnt vmcnt(0)
	v_add_f32_e32 v25, v25, v0
	v_add_f32_e32 v0, v9, v0
	v_exp_f32_e32 v9, v86
	v_exp_f32_e32 v86, v88
	v_fmamk_f32 v88, v83, 0x3f07dc22, v126
	v_fmamk_f32 v89, v87, 0x3f07dc22, v126
	v_fmaak_f32 v88, v83, v88, 0x3f35f0e3
	v_fmaak_f32 v89, v87, v89, 0x3f35f0e3
	v_fmaak_f32 v88, v83, v88, 0xbe11a98e
	v_fmaak_f32 v89, v87, v89, 0xbe11a98e
	v_fmaak_f32 v88, v83, v88, 0x3e027906
	v_fmaak_f32 v89, v87, v89, 0x3e027906
	v_mul_f32_e32 v83, v83, v88
	v_mul_f32_e32 v87, v87, v89
	v_mul_f32_e32 v9, v9, v83
	v_mul_f32_e32 v83, v86, v87
	v_mul_f32_e32 v86, v9, v1
	v_fma_f32 v9, -v9, v1, v1
	v_cmp_gt_f32_e32 vcc, 0, v1
	v_mul_f32_e32 v87, v83, v82
	v_fma_f32 v83, -v83, v82, v82
	v_cndmask_b32_e32 v1, v9, v86, vcc
	v_cmp_gt_f32_e32 vcc, 0, v82
	v_mul_f32_e32 v25, v25, v1
	s_nop 0
	v_cndmask_b32_e32 v9, v83, v87, vcc
	v_mul_f32_e32 v9, v0, v9
	v_mul_f32_e32 v0, v9, v9
	v_fmac_f32_e32 v0, v25, v25
	s_nop 1
	s_waitcnt lgkmcnt(0)
	v_add_f32_dpp v0, v0, v0 quad_perm:[1,0,3,2] row_mask:0xf bank_mask:0xf
	s_nop 1
	s_waitcnt lgkmcnt(0)
	v_add_f32_dpp v0, v0, v0 quad_perm:[2,3,0,1] row_mask:0xf bank_mask:0xf
	s_nop 1
	s_waitcnt lgkmcnt(0)
	v_add_f32_dpp v0, v0, v0 row_half_mirror row_mask:0xf bank_mask:0xf
	s_nop 1
	s_waitcnt lgkmcnt(0)
	v_add_f32_dpp v0, v0, v0 row_mirror row_mask:0xf bank_mask:0xf
	ds_swizzle_b32 v1, v0 offset:swizzle(SWAP,16)
	s_and_saveexec_b64 s[4:5], s[0:1]
	s_cbranch_execz .LBB0_199
	s_waitcnt lgkmcnt(0)
	v_add_f32_e32 v0, v0, v1
	v_add_u32_e32 v1, s25, v113
	ds_write_b32 v1, v0 offset:32768
; __device__ __forceinline__ float bf16_lo(unsigned u) { return __uint_as_float(u << 16); }
; __device__ __forceinline__ float bf16_hi(unsigned u) { return __uint_as_float(u & 0xffff0000u); }
; __device__ __forceinline__ float gelu_f(float v) {
;     const float av = fabsf(v), dd = av * 0.2316418882f + 1.0f;
;     const float tt = __builtin_amdgcn_rcpf(dd);
;     float q = tt * 0.5307027145f + (-0.7265760135f); q = q * tt + 0.7107068705f; q = q * tt + (-0.142248368f); q = q * tt + 0.127414796f; q = q * tt;
;     const float e = __builtin_amdgcn_exp2f((v * v) * (-0.72134752044f));
;     const float m = v * (q * e);
;     return v < 0.f ? m : v - m;
; __device__ __forceinline__ void phase_mixer(const Params& p, LAS3 char* lds, int wid) {
;     ...
;                 for (int r = 0; r < 16; ++r) {
;                     const int tt = 32 * mt + (r & 3) + 8 * (r >> 2) + 4 * kh;
;                     const unsigned uu = *(const unsigned*)(ub + (size_t)tt * DIN);
;                     const float bias = p.sgu_b[hd * 128 + tt];
;                     ya[r] = gelu_f(bf16_lo(uu)) * (acc0[r] + bias);
;                     yb[r] = gelu_f(bf16_hi(uu)) * (acc1[r] + bias);
;                     const float ps = half_sum32(ya[r] * ya[r] + yb[r] * yb[r]);
;                     if (n == 0) stat[tt * 2 + (wid & 1)] = ps;
;                 }
.LBB0_199:
	s_or_b64 exec, exec, s[4:5]
	s_waitcnt lgkmcnt(0)
	v_lshl_add_u64 v[0:1], v[80:81], 0, v[64:65]
	v_add_u32_e32 v0, s92, v114
	v_ashrrev_i32_e32 v1, 31, v0
	v_lshl_add_u64 v[0:1], v[0:1], 2, s[98:99]
	v_mov_b32_e32 v0, v226
	s_waitcnt vmcnt(0)
	v_mov_b32_e32 v82, v210
	v_lshlrev_b32_e32 v1, 16, v82
	v_and_b32_e32 v82, 0xffff0000, v82
	v_fma_f32 v83, |v1|, s87, 1.0
	v_fma_f32 v87, |v82|, s87, 1.0
	v_rcp_f32_e32 v83, v83
	v_rcp_f32_e32 v87, v87
	v_mul_f32_e32 v86, v1, v1
	v_mul_f32_e32 v88, v82, v82
	v_mul_f32_e32 v86, 0xbf38aa3b, v86
	v_mul_f32_e32 v88, 0xbf38aa3b, v88
	s_waitcnt vmcnt(0)
	v_add_f32_e32 v26, v26, v0
	v_add_f32_e32 v0, v10, v0
	v_exp_f32_e32 v10, v86
	v_exp_f32_e32 v86, v88
	v_fmamk_f32 v88, v83, 0x3f07dc22, v126
	v_fmamk_f32 v89, v87, 0x3f07dc22, v126
	v_fmaak_f32 v88, v83, v88, 0x3f35f0e3
	v_fmaak_f32 v89, v87, v89, 0x3f35f0e3
	v_fmaak_f32 v88, v83, v88, 0xbe11a98e
	v_fmaak_f32 v89, v87, v89, 0xbe11a98e
	v_fmaak_f32 v88, v83, v88, 0x3e027906
	v_fmaak_f32 v89, v87, v89, 0x3e027906
	v_mul_f32_e32 v83, v83, v88
	v_mul_f32_e32 v87, v87, v89
	v_mul_f32_e32 v10, v10, v83
	v_mul_f32_e32 v83, v86, v87
	v_mul_f32_e32 v86, v10, v1
	v_fma_f32 v10, -v10, v1, v1
	v_cmp_gt_f32_e32 vcc, 0, v1
	v_mul_f32_e32 v87, v83, v82
	v_fma_f32 v83, -v83, v82, v82
	v_cndmask_b32_e32 v1, v10, v86, vcc
	v_cmp_gt_f32_e32 vcc, 0, v82
	v_mul_f32_e32 v26, v26, v1
	s_nop 0
	v_cndmask_b32_e32 v10, v83, v87, vcc
	v_mul_f32_e32 v10, v0, v10
	v_mul_f32_e32 v0, v10, v10
	v_fmac_f32_e32 v0, v26, v26
	s_nop 1
	s_waitcnt lgkmcnt(0)
	v_add_f32_dpp v0, v0, v0 quad_perm:[1,0,3,2] row_mask:0xf bank_mask:0xf
	s_nop 1
	s_waitcnt lgkmcnt(0)
	v_add_f32_dpp v0, v0, v0 quad_perm:[2,3,0,1] row_mask:0xf bank_mask:0xf
	s_nop 1
	s_waitcnt lgkmcnt(0)
	v_add_f32_dpp v0, v0, v0 row_half_mirror row_mask:0xf bank_mask:0xf
	s_nop 1
	s_waitcnt lgkmcnt(0)
	v_add_f32_dpp v0, v0, v0 row_mirror row_mask:0xf bank_mask:0xf
	ds_swizzle_b32 v1, v0 offset:swizzle(SWAP,16)
	s_and_saveexec_b64 s[4:5], s[0:1]
	s_cbranch_execz .LBB0_201
	s_waitcnt lgkmcnt(0)
	v_add_f32_e32 v0, v0, v1
	v_add_u32_e32 v1, s25, v115
	ds_write_b32 v1, v0 offset:32768
.LBB0_201:
	s_or_b64 exec, exec, s[4:5]
	s_waitcnt lgkmcnt(0)
	v_lshl_add_u64 v[0:1], v[80:81], 0, v[66:67]
	v_add_u32_e32 v0, s92, v116
	v_ashrrev_i32_e32 v1, 31, v0
	v_lshl_add_u64 v[0:1], v[0:1], 2, s[98:99]
	v_mov_b32_e32 v0, v227
	s_waitcnt vmcnt(0)
	v_mov_b32_e32 v82, v211
	v_lshlrev_b32_e32 v1, 16, v82
	v_and_b32_e32 v82, 0xffff0000, v82
	v_fma_f32 v83, |v1|, s87, 1.0
	v_fma_f32 v87, |v82|, s87, 1.0
	v_rcp_f32_e32 v83, v83
	v_rcp_f32_e32 v87, v87
	v_mul_f32_e32 v86, v1, v1
	v_mul_f32_e32 v88, v82, v82
	v_mul_f32_e32 v86, 0xbf38aa3b, v86
	v_mul_f32_e32 v88, 0xbf38aa3b, v88
	s_waitcnt vmcnt(0)
	v_add_f32_e32 v27, v27, v0
	v_add_f32_e32 v0, v11, v0
	v_exp_f32_e32 v11, v86
	v_exp_f32_e32 v86, v88
	v_fmamk_f32 v88, v83, 0x3f07dc22, v126
	v_fmamk_f32 v89, v87, 0x3f07dc22, v126
	v_fmaak_f32 v88, v83, v88, 0x3f35f0e3
	v_fmaak_f32 v89, v87, v89, 0x3f35f0e3
	v_fmaak_f32 v88, v83, v88, 0xbe11a98e
	v_fmaak_f32 v89, v87, v89, 0xbe11a98e
	v_fmaak_f32 v88, v83, v88, 0x3e027906
	v_fmaak_f32 v89, v87, v89, 0x3e027906
	v_mul_f32_e32 v83, v83, v88
	v_mul_f32_e32 v87, v87, v89
	v_mul_f32_e32 v11, v11, v83
	v_mul_f32_e32 v83, v86, v87
	v_mul_f32_e32 v86, v11, v1
	v_fma_f32 v11, -v11, v1, v1
	v_cmp_gt_f32_e32 vcc, 0, v1
	v_mul_f32_e32 v87, v83, v82
	v_fma_f32 v83, -v83, v82, v82
	v_cndmask_b32_e32 v1, v11, v86, vcc
	v_cmp_gt_f32_e32 vcc, 0, v82
	v_mul_f32_e32 v27, v27, v1
	s_nop 0
	v_cndmask_b32_e32 v11, v83, v87, vcc
	v_mul_f32_e32 v11, v0, v11
	v_mul_f32_e32 v0, v11, v11
	v_fmac_f32_e32 v0, v27, v27
	s_nop 1
	s_waitcnt lgkmcnt(0)
	v_add_f32_dpp v0, v0, v0 quad_perm:[1,0,3,2] row_mask:0xf bank_mask:0xf
	s_nop 1
	s_waitcnt lgkmcnt(0)
	v_add_f32_dpp v0, v0, v0 quad_perm:[2,3,0,1] row_mask:0xf bank_mask:0xf
	s_nop 1
	s_waitcnt lgkmcnt(0)
	v_add_f32_dpp v0, v0, v0 row_half_mirror row_mask:0xf bank_mask:0xf
	s_nop 1
	s_waitcnt lgkmcnt(0)
	v_add_f32_dpp v0, v0, v0 row_mirror row_mask:0xf bank_mask:0xf
	ds_swizzle_b32 v1, v0 offset:swizzle(SWAP,16)
	s_and_saveexec_b64 s[4:5], s[0:1]
	s_cbranch_execz .LBB0_203
	s_waitcnt lgkmcnt(0)
	v_add_f32_e32 v0, v0, v1
	v_add_u32_e32 v1, s25, v117
	ds_write_b32 v1, v0 offset:32768
.LBB0_203:
	s_or_b64 exec, exec, s[4:5]
	s_waitcnt lgkmcnt(0)
	v_lshl_add_u64 v[0:1], v[80:81], 0, v[68:69]
	v_add_u32_e32 v0, s92, v118
	v_ashrrev_i32_e32 v1, 31, v0
	v_lshl_add_u64 v[0:1], v[0:1], 2, s[98:99]
	v_mov_b32_e32 v0, v228
	s_waitcnt vmcnt(0)
	v_mov_b32_e32 v82, v212
	v_lshlrev_b32_e32 v1, 16, v82
	v_and_b32_e32 v82, 0xffff0000, v82
	v_fma_f32 v83, |v1|, s87, 1.0
	v_fma_f32 v87, |v82|, s87, 1.0
	v_rcp_f32_e32 v83, v83
	v_rcp_f32_e32 v87, v87
	v_mul_f32_e32 v86, v1, v1
	v_mul_f32_e32 v88, v82, v82
	v_mul_f32_e32 v86, 0xbf38aa3b, v86
	v_mul_f32_e32 v88, 0xbf38aa3b, v88
	s_waitcnt vmcnt(0)
	v_add_f32_e32 v28, v28, v0
	v_add_f32_e32 v0, v12, v0
	v_exp_f32_e32 v12, v86
	v_exp_f32_e32 v86, v88
	v_fmamk_f32 v88, v83, 0x3f07dc22, v126
	v_fmamk_f32 v89, v87, 0x3f07dc22, v126
	v_fmaak_f32 v88, v83, v88, 0x3f35f0e3
	v_fmaak_f32 v89, v87, v89, 0x3f35f0e3
	v_fmaak_f32 v88, v83, v88, 0xbe11a98e
	v_fmaak_f32 v89, v87, v89, 0xbe11a98e
	v_fmaak_f32 v88, v83, v88, 0x3e027906
	v_fmaak_f32 v89, v87, v89, 0x3e027906
	v_mul_f32_e32 v83, v83, v88
	v_mul_f32_e32 v87, v87, v89
	v_mul_f32_e32 v12, v12, v83
	v_mul_f32_e32 v83, v86, v87
	v_mul_f32_e32 v86, v12, v1
	v_fma_f32 v12, -v12, v1, v1
	v_cmp_gt_f32_e32 vcc, 0, v1
	v_mul_f32_e32 v87, v83, v82
	v_fma_f32 v83, -v83, v82, v82
	v_cndmask_b32_e32 v1, v12, v86, vcc
	v_cmp_gt_f32_e32 vcc, 0, v82
	v_mul_f32_e32 v28, v28, v1
	s_nop 0
	v_cndmask_b32_e32 v12, v83, v87, vcc
	v_mul_f32_e32 v12, v0, v12
	v_mul_f32_e32 v0, v12, v12
	v_fmac_f32_e32 v0, v28, v28
	s_nop 1
	s_waitcnt lgkmcnt(0)
	v_add_f32_dpp v0, v0, v0 quad_perm:[1,0,3,2] row_mask:0xf bank_mask:0xf
	s_nop 1
	s_waitcnt lgkmcnt(0)
	v_add_f32_dpp v0, v0, v0 quad_perm:[2,3,0,1] row_mask:0xf bank_mask:0xf
	s_nop 1
	s_waitcnt lgkmcnt(0)
	v_add_f32_dpp v0, v0, v0 row_half_mirror row_mask:0xf bank_mask:0xf
	s_nop 1
	s_waitcnt lgkmcnt(0)
	v_add_f32_dpp v0, v0, v0 row_mirror row_mask:0xf bank_mask:0xf
	ds_swizzle_b32 v1, v0 offset:swizzle(SWAP,16)
	s_and_saveexec_b64 s[4:5], s[0:1]
	s_cbranch_execz .LBB0_205
	s_waitcnt lgkmcnt(0)
	v_add_f32_e32 v0, v0, v1
	v_add_u32_e32 v1, s25, v119
	ds_write_b32 v1, v0 offset:32768
; __device__ __forceinline__ float bf16_lo(unsigned u) { return __uint_as_float(u << 16); }
; __device__ __forceinline__ float bf16_hi(unsigned u) { return __uint_as_float(u & 0xffff0000u); }
; __device__ __forceinline__ float gelu_f(float v) {
;     const float av = fabsf(v), dd = av * 0.2316418882f + 1.0f;
;     const float tt = __builtin_amdgcn_rcpf(dd);
;     float q = tt * 0.5307027145f + (-0.7265760135f); q = q * tt + 0.7107068705f; q = q * tt + (-0.142248368f); q = q * tt + 0.127414796f; q = q * tt;
;     const float e = __builtin_amdgcn_exp2f((v * v) * (-0.72134752044f));
;     const float m = v * (q * e);
;     return v < 0.f ? m : v - m;
; __device__ __forceinline__ void phase_mixer(const Params& p, LAS3 char* lds, int wid) {
;     ...
;                 for (int r = 0; r < 16; ++r) {
;                     const int tt = 32 * mt + (r & 3) + 8 * (r >> 2) + 4 * kh;
;                     const unsigned uu = *(const unsigned*)(ub + (size_t)tt * DIN);
;                     const float bias = p.sgu_b[hd * 128 + tt];
;                     ya[r] = gelu_f(bf16_lo(uu)) * (acc0[r] + bias);
;                     yb[r] = gelu_f(bf16_hi(uu)) * (acc1[r] + bias);
;                     const float ps = half_sum32(ya[r] * ya[r] + yb[r] * yb[r]);
;                     if (n == 0) stat[tt * 2 + (wid & 1)] = ps;
;                 }
.LBB0_205:
	s_or_b64 exec, exec, s[4:5]
	s_waitcnt lgkmcnt(0)
	v_lshl_add_u64 v[0:1], v[80:81], 0, v[70:71]
	v_add_u32_e32 v0, s92, v120
	v_ashrrev_i32_e32 v1, 31, v0
	v_lshl_add_u64 v[0:1], v[0:1], 2, s[98:99]
	v_mov_b32_e32 v0, v229
	s_waitcnt vmcnt(0)
	v_mov_b32_e32 v82, v213
	v_lshlrev_b32_e32 v1, 16, v82
	v_and_b32_e32 v82, 0xffff0000, v82
	v_fma_f32 v83, |v1|, s87, 1.0
	v_fma_f32 v87, |v82|, s87, 1.0
	v_rcp_f32_e32 v83, v83
	v_rcp_f32_e32 v87, v87
	v_mul_f32_e32 v86, v1, v1
	v_mul_f32_e32 v88, v82, v82
	v_mul_f32_e32 v86, 0xbf38aa3b, v86
	v_mul_f32_e32 v88, 0xbf38aa3b, v88
	s_waitcnt vmcnt(0)
	v_add_f32_e32 v29, v29, v0
	v_add_f32_e32 v0, v13, v0
	v_exp_f32_e32 v13, v86
	v_exp_f32_e32 v86, v88
	v_fmamk_f32 v88, v83, 0x3f07dc22, v126
	v_fmamk_f32 v89, v87, 0x3f07dc22, v126
	v_fmaak_f32 v88, v83, v88, 0x3f35f0e3
	v_fmaak_f32 v89, v87, v89, 0x3f35f0e3
	v_fmaak_f32 v88, v83, v88, 0xbe11a98e
	v_fmaak_f32 v89, v87, v89, 0xbe11a98e
	v_fmaak_f32 v88, v83, v88, 0x3e027906
	v_fmaak_f32 v89, v87, v89, 0x3e027906
	v_mul_f32_e32 v83, v83, v88
	v_mul_f32_e32 v87, v87, v89
	v_mul_f32_e32 v13, v13, v83
	v_mul_f32_e32 v83, v86, v87
	v_mul_f32_e32 v86, v13, v1
	v_fma_f32 v13, -v13, v1, v1
	v_cmp_gt_f32_e32 vcc, 0, v1
	v_mul_f32_e32 v87, v83, v82
	v_fma_f32 v83, -v83, v82, v82
	v_cndmask_b32_e32 v1, v13, v86, vcc
	v_cmp_gt_f32_e32 vcc, 0, v82
	v_mul_f32_e32 v29, v29, v1
	s_nop 0
	v_cndmask_b32_e32 v13, v83, v87, vcc
	v_mul_f32_e32 v13, v0, v13
	v_mul_f32_e32 v0, v13, v13
	v_fmac_f32_e32 v0, v29, v29
	s_nop 1
	s_waitcnt lgkmcnt(0)
	v_add_f32_dpp v0, v0, v0 quad_perm:[1,0,3,2] row_mask:0xf bank_mask:0xf
	s_nop 1
	s_waitcnt lgkmcnt(0)
	v_add_f32_dpp v0, v0, v0 quad_perm:[2,3,0,1] row_mask:0xf bank_mask:0xf
	s_nop 1
	s_waitcnt lgkmcnt(0)
	v_add_f32_dpp v0, v0, v0 row_half_mirror row_mask:0xf bank_mask:0xf
	s_nop 1
	s_waitcnt lgkmcnt(0)
	v_add_f32_dpp v0, v0, v0 row_mirror row_mask:0xf bank_mask:0xf
	ds_swizzle_b32 v1, v0 offset:swizzle(SWAP,16)
	s_and_saveexec_b64 s[4:5], s[0:1]
	s_cbranch_execz .LBB0_207
	s_waitcnt lgkmcnt(0)
	v_add_f32_e32 v0, v0, v1
	v_add_u32_e32 v1, s25, v121
	ds_write_b32 v1, v0 offset:32768
.LBB0_207:
	s_or_b64 exec, exec, s[4:5]
	s_waitcnt lgkmcnt(0)
	v_lshl_add_u64 v[0:1], v[80:81], 0, v[72:73]
	v_add_u32_e32 v0, s92, v122
	v_ashrrev_i32_e32 v1, 31, v0
	v_lshl_add_u64 v[0:1], v[0:1], 2, s[98:99]
	v_mov_b32_e32 v0, v230
	s_waitcnt vmcnt(0)
	v_mov_b32_e32 v82, v214
	v_lshlrev_b32_e32 v1, 16, v82
	v_and_b32_e32 v82, 0xffff0000, v82
	v_fma_f32 v83, |v1|, s87, 1.0
	v_fma_f32 v87, |v82|, s87, 1.0
	v_rcp_f32_e32 v83, v83
	v_rcp_f32_e32 v87, v87
	v_mul_f32_e32 v86, v1, v1
	v_mul_f32_e32 v88, v82, v82
	v_mul_f32_e32 v86, 0xbf38aa3b, v86
	v_mul_f32_e32 v88, 0xbf38aa3b, v88
	s_waitcnt vmcnt(0)
	v_add_f32_e32 v30, v30, v0
	v_add_f32_e32 v0, v14, v0
	v_exp_f32_e32 v14, v86
	v_exp_f32_e32 v86, v88
	v_fmamk_f32 v88, v83, 0x3f07dc22, v126
	v_fmamk_f32 v89, v87, 0x3f07dc22, v126
	v_fmaak_f32 v88, v83, v88, 0x3f35f0e3
	v_fmaak_f32 v89, v87, v89, 0x3f35f0e3
	v_fmaak_f32 v88, v83, v88, 0xbe11a98e
	v_fmaak_f32 v89, v87, v89, 0xbe11a98e
	v_fmaak_f32 v88, v83, v88, 0x3e027906
	v_fmaak_f32 v89, v87, v89, 0x3e027906
	v_mul_f32_e32 v83, v83, v88
	v_mul_f32_e32 v87, v87, v89
	v_mul_f32_e32 v14, v14, v83
	v_mul_f32_e32 v83, v86, v87
	v_mul_f32_e32 v86, v14, v1
	v_fma_f32 v14, -v14, v1, v1
	v_cmp_gt_f32_e32 vcc, 0, v1
	v_mul_f32_e32 v87, v83, v82
	v_fma_f32 v83, -v83, v82, v82
	v_cndmask_b32_e32 v1, v14, v86, vcc
	v_cmp_gt_f32_e32 vcc, 0, v82
	v_mul_f32_e32 v30, v30, v1
	s_nop 0
	v_cndmask_b32_e32 v14, v83, v87, vcc
	v_mul_f32_e32 v14, v0, v14
	v_mul_f32_e32 v0, v14, v14
	v_fmac_f32_e32 v0, v30, v30
	s_nop 1
	s_waitcnt lgkmcnt(0)
	v_add_f32_dpp v0, v0, v0 quad_perm:[1,0,3,2] row_mask:0xf bank_mask:0xf
	s_nop 1
	s_waitcnt lgkmcnt(0)
	v_add_f32_dpp v0, v0, v0 quad_perm:[2,3,0,1] row_mask:0xf bank_mask:0xf
	s_nop 1
	s_waitcnt lgkmcnt(0)
	v_add_f32_dpp v0, v0, v0 row_half_mirror row_mask:0xf bank_mask:0xf
	s_nop 1
	s_waitcnt lgkmcnt(0)
	v_add_f32_dpp v0, v0, v0 row_mirror row_mask:0xf bank_mask:0xf
	ds_swizzle_b32 v1, v0 offset:swizzle(SWAP,16)
	s_and_saveexec_b64 s[4:5], s[0:1]
	s_cbranch_execz .LBB0_209
	s_waitcnt lgkmcnt(0)
	v_add_f32_e32 v0, v0, v1
	v_add_u32_e32 v1, s25, v123
	ds_write_b32 v1, v0 offset:32768
.LBB0_209:
	s_or_b64 exec, exec, s[4:5]
	s_waitcnt lgkmcnt(0)
	v_lshl_add_u64 v[0:1], v[80:81], 0, v[74:75]
	v_add_u32_e32 v0, s92, v124
	v_ashrrev_i32_e32 v1, 31, v0
	v_lshl_add_u64 v[0:1], v[0:1], 2, s[98:99]
	v_mov_b32_e32 v0, v231
	s_waitcnt vmcnt(0)
	v_mov_b32_e32 v80, v215
	v_lshlrev_b32_e32 v1, 16, v80
	v_and_b32_e32 v80, 0xffff0000, v80
	v_fma_f32 v81, |v1|, s87, 1.0
	v_fma_f32 v83, |v80|, s87, 1.0
	v_rcp_f32_e32 v81, v81
	v_rcp_f32_e32 v83, v83
	v_mul_f32_e32 v82, v1, v1
	v_mul_f32_e32 v86, v80, v80
	v_mul_f32_e32 v82, 0xbf38aa3b, v82
	v_mul_f32_e32 v86, 0xbf38aa3b, v86
	s_waitcnt vmcnt(0)
	v_add_f32_e32 v31, v31, v0
	v_add_f32_e32 v0, v15, v0
	v_exp_f32_e32 v15, v82
	v_exp_f32_e32 v82, v86
	v_fmamk_f32 v86, v81, 0x3f07dc22, v126
	v_fmamk_f32 v87, v83, 0x3f07dc22, v126
	v_fmaak_f32 v86, v81, v86, 0x3f35f0e3
	v_fmaak_f32 v87, v83, v87, 0x3f35f0e3
	v_fmaak_f32 v86, v81, v86, 0xbe11a98e
	v_fmaak_f32 v87, v83, v87, 0xbe11a98e
	v_fmaak_f32 v86, v81, v86, 0x3e027906
	v_fmaak_f32 v87, v83, v87, 0x3e027906
	v_mul_f32_e32 v81, v81, v86
	v_mul_f32_e32 v83, v83, v87
	v_mul_f32_e32 v15, v15, v81
	v_mul_f32_e32 v81, v82, v83
	v_mul_f32_e32 v82, v15, v1
	v_fma_f32 v15, -v15, v1, v1
	v_cmp_gt_f32_e32 vcc, 0, v1
	v_mul_f32_e32 v83, v81, v80
	v_fma_f32 v81, -v81, v80, v80
	v_cndmask_b32_e32 v1, v15, v82, vcc
	v_cmp_gt_f32_e32 vcc, 0, v80
	v_mul_f32_e32 v31, v31, v1
	s_nop 0
	v_cndmask_b32_e32 v15, v81, v83, vcc
	v_mul_f32_e32 v15, v0, v15
	v_mul_f32_e32 v0, v15, v15
	v_fmac_f32_e32 v0, v31, v31
	s_nop 1
	s_waitcnt lgkmcnt(0)
	v_add_f32_dpp v0, v0, v0 quad_perm:[1,0,3,2] row_mask:0xf bank_mask:0xf
	s_nop 1
	s_waitcnt lgkmcnt(0)
	v_add_f32_dpp v0, v0, v0 quad_perm:[2,3,0,1] row_mask:0xf bank_mask:0xf
	s_nop 1
	s_waitcnt lgkmcnt(0)
	v_add_f32_dpp v0, v0, v0 row_half_mirror row_mask:0xf bank_mask:0xf
	s_nop 1
	s_waitcnt lgkmcnt(0)
	v_add_f32_dpp v0, v0, v0 row_mirror row_mask:0xf bank_mask:0xf
	ds_swizzle_b32 v1, v0 offset:swizzle(SWAP,16)
	s_and_saveexec_b64 s[4:5], s[0:1]
	s_cbranch_execz .LBB0_211
	s_waitcnt lgkmcnt(0)
	v_add_f32_e32 v0, v0, v1
	v_add_u32_e32 v1, s25, v125
	ds_write_b32 v1, v0 offset:32768
